# final combine+rmsnorm: wave sum by DPP quad/row mirrors + permlane16/32 swaps (same xor-butterfly order, bit-identical) instead of 6 serial ds_bpermute round trips per row
# baseline (speedup 1.0000x reference)
.LBB0_2192:
	s_add_i32 s0, s8, -3
	s_ashr_i32 s1, s0, 31
	s_lshl_b64 s[0:1], s[0:1], 2
	s_add_u32 s20, s14, s0
	s_addc_u32 s21, s15, s1
	s_add_u32 s0, s16, s0
	s_addc_u32 s1, s17, s1
	global_load_dwordx2 v[22:23], v[16:17], off offset:512
	global_load_dwordx2 v[24:25], v[16:17], off offset:1024
	global_load_dwordx2 v[28:29], v[16:17], off offset:1536
	global_load_dwordx2 v[26:27], v[16:17], off
	global_load_dword v39, v36, s[20:21]
	global_load_dword v40, v36, s[0:1]
	s_add_i32 s20, s8, -2
	s_ashr_i32 s21, s20, 31
	s_lshl_b64 s[0:1], s[20:21], 2
	s_add_u32 s20, s14, s0
	s_addc_u32 s21, s15, s1
	s_add_u32 s0, s16, s0
	s_addc_u32 s1, s17, s1
	global_load_dword v43, v36, s[20:21]
	global_load_dword v42, v36, s[0:1]
	s_add_i32 s20, s8, -1
	s_ashr_i32 s21, s20, 31
	s_lshl_b64 s[0:1], s[20:21], 2
	s_add_u32 s20, s14, s0
	s_addc_u32 s21, s15, s1
	global_load_dword v45, v36, s[20:21]
	s_add_u32 s0, s16, s0
	s_addc_u32 s1, s17, s1
	s_ashr_i32 s9, s8, 31
	global_load_dword v44, v36, s[0:1]
	s_lshl_b64 s[0:1], s[8:9], 2
	s_add_u32 s20, s14, s0
	s_addc_u32 s21, s15, s1
	global_load_dword v47, v36, s[20:21]
	s_add_u32 s0, s16, s0
	s_addc_u32 s1, s17, s1
	global_load_dword v46, v36, s[0:1]
	s_add_i32 s2, s2, s6
	s_add_i32 s8, s8, s18
	v_lshl_add_u64 v[16:17], v[16:17], 0, s[10:11]
	s_cmpk_lt_i32 s2, 0x4000
	s_waitcnt vmcnt(11)
	v_lshlrev_b32_e32 v48, 16, v22
	s_waitcnt vmcnt(10)
	v_lshlrev_b32_e32 v63, 16, v25
	s_waitcnt vmcnt(9)
	v_lshlrev_b32_e32 v64, 16, v28
	v_and_b32_e32 v49, 0xffff0000, v28
	s_waitcnt vmcnt(7)
	v_lshlrev_b32_e32 v28, 2, v39
	v_add_u32_e32 v28, s3, v28
	ds_read_b32 v54, v28 offset:128
	s_waitcnt vmcnt(6)
	v_ashrrev_i32_e32 v41, 31, v40
	v_lshlrev_b64 v[40:41], 10, v[40:41]
	v_lshlrev_b32_e32 v52, 16, v26
	v_and_b32_e32 v53, 0xffff0000, v26
	s_waitcnt lgkmcnt(0)
	v_ashrrev_i32_e32 v55, 31, v54
	v_lshlrev_b64 v[54:55], 18, v[54:55]
	s_waitcnt vmcnt(5)
	v_lshlrev_b32_e32 v28, 2, v43
	v_add_u32_e32 v28, s3, v28
	ds_read_b32 v56, v28 offset:128
	v_lshl_add_u64 v[54:55], s[4:5], 0, v[54:55]
	v_lshl_add_u64 v[40:41], v[54:55], 0, v[40:41]
	v_lshl_add_u64 v[40:41], v[40:41], 0, v[20:21]
	global_load_dword v39, v[40:41], off
	global_load_dword v58, v[40:41], off offset:256
	global_load_dword v59, v[40:41], off offset:512
	global_load_dword v60, v[40:41], off offset:768
	s_waitcnt vmcnt(7)
	v_lshlrev_b32_e32 v28, 2, v45
	v_add_u32_e32 v28, s3, v28
	ds_read_b32 v40, v28 offset:128
	s_waitcnt lgkmcnt(1)
	v_ashrrev_i32_e32 v57, 31, v56
	v_ashrrev_i32_e32 v43, 31, v42
	v_lshlrev_b64 v[54:55], 18, v[56:57]
	v_lshlrev_b64 v[42:43], 10, v[42:43]
	v_lshl_add_u64 v[54:55], s[4:5], 0, v[54:55]
	v_lshl_add_u64 v[42:43], v[54:55], 0, v[42:43]
	s_waitcnt vmcnt(5)
	v_lshlrev_b32_e32 v28, 2, v47
	v_lshl_add_u64 v[42:43], v[42:43], 0, v[20:21]
	v_add_u32_e32 v28, s3, v28
	s_waitcnt lgkmcnt(0)
	v_ashrrev_i32_e32 v41, 31, v40
	v_ashrrev_i32_e32 v45, 31, v44
	global_load_dword v65, v[42:43], off
	global_load_dword v66, v[42:43], off offset:256
	global_load_dword v67, v[42:43], off offset:512
	global_load_dword v68, v[42:43], off offset:768
	ds_read_b32 v42, v28 offset:128
	v_lshlrev_b64 v[40:41], 18, v[40:41]
	v_lshlrev_b64 v[44:45], 10, v[44:45]
	v_lshl_add_u64 v[40:41], s[4:5], 0, v[40:41]
	v_lshl_add_u64 v[40:41], v[40:41], 0, v[44:45]
	v_lshl_add_u64 v[40:41], v[40:41], 0, v[20:21]
	global_load_dword v69, v[40:41], off
	global_load_dword v70, v[40:41], off offset:256
	global_load_dword v71, v[40:41], off offset:512
	global_load_dword v74, v[40:41], off offset:768
	s_waitcnt lgkmcnt(0)
	v_ashrrev_i32_e32 v43, 31, v42
	s_waitcnt vmcnt(12)
	v_ashrrev_i32_e32 v47, 31, v46
	v_lshlrev_b64 v[40:41], 18, v[42:43]
	v_lshlrev_b64 v[46:47], 10, v[46:47]
	v_lshl_add_u64 v[40:41], s[4:5], 0, v[40:41]
	v_lshl_add_u64 v[40:41], v[40:41], 0, v[46:47]
	v_lshl_add_u64 v[40:41], v[40:41], 0, v[20:21]
	global_load_dword v76, v[40:41], off
	global_load_dword v77, v[40:41], off offset:256
	global_load_dword v78, v[40:41], off offset:512
	global_load_dword v79, v[40:41], off offset:768
	v_lshlrev_b32_e32 v26, 16, v27
	v_and_b32_e32 v27, 0xffff0000, v27
	v_and_b32_e32 v50, 0xffff0000, v23
	v_lshlrev_b32_e32 v62, 16, v24
	v_and_b32_e32 v22, 0xffff0000, v22
	v_lshlrev_b32_e32 v23, 16, v23
	v_and_b32_e32 v25, 0xffff0000, v25
	v_and_b32_e32 v24, 0xffff0000, v24
	v_lshlrev_b32_e32 v51, 16, v29
	v_and_b32_e32 v29, 0xffff0000, v29
	s_waitcnt vmcnt(15)
	v_cvt_pk_f32_fp8_sdwa v[42:43], v39 src0_sel:WORD_1
	s_waitcnt vmcnt(14)
	v_cvt_pk_f32_fp8_e32 v[44:45], v58
	v_cvt_pk_f32_fp8_sdwa v[46:47], v58 src0_sel:WORD_1
	s_waitcnt vmcnt(13)
	v_cvt_pk_f32_fp8_e32 v[54:55], v59
	v_cvt_pk_f32_fp8_sdwa v[56:57], v59 src0_sel:WORD_1
	v_cvt_pk_f32_fp8_e32 v[40:41], v39
	v_pk_add_f32 v[26:27], v[42:43], v[26:27]
	v_pk_mov_b32 v[42:43], v[44:45], v[46:47] op_sel:[1,0]
	v_add_f32_e32 v28, v56, v63
	v_mov_b32_e32 v56, v55
	s_waitcnt vmcnt(12)
	v_cvt_pk_f32_fp8_e32 v[58:59], v60
	v_cvt_pk_f32_fp8_sdwa v[60:61], v60 src0_sel:WORD_1
	v_add_f32_e32 v39, v44, v48
	v_add_f32_e32 v72, v47, v50
	v_add_f32_e32 v50, v54, v62
	v_pk_add_f32 v[40:41], v[40:41], v[52:53]
	v_pk_add_f32 v[22:23], v[42:43], v[22:23]
	v_pk_add_f32 v[24:25], v[56:57], v[24:25]
	s_waitcnt vmcnt(11)
	v_cvt_pk_f32_fp8_e32 v[42:43], v65
	v_cvt_pk_f32_fp8_sdwa v[44:45], v65 src0_sel:WORD_1
	s_waitcnt vmcnt(10)
	v_cvt_pk_f32_fp8_e32 v[46:47], v66
	v_cvt_pk_f32_fp8_sdwa v[52:53], v66 src0_sel:WORD_1
	s_waitcnt vmcnt(9)
	v_cvt_pk_f32_fp8_e32 v[54:55], v67
	v_cvt_pk_f32_fp8_sdwa v[56:57], v67 src0_sel:WORD_1
	s_waitcnt vmcnt(8)
	v_cvt_pk_f32_fp8_e32 v[62:63], v68
	v_add_f32_e32 v48, v39, v46
	v_add_f32_e32 v39, v72, v53
	v_pk_add_f32 v[40:41], v[40:41], v[42:43]
	v_pk_add_f32 v[26:27], v[26:27], v[44:45]
	v_pk_mov_b32 v[42:43], v[46:47], v[52:53] op_sel:[1,0]
	v_mov_b32_e32 v44, v55
	v_mov_b32_e32 v45, v57
	v_mov_b32_e32 v55, v60
	v_mov_b32_e32 v57, v61
	s_waitcnt vmcnt(7)
	v_cvt_pk_f32_fp8_e32 v[46:47], v69
	v_cvt_pk_f32_fp8_sdwa v[52:53], v69 src0_sel:WORD_1
	s_waitcnt vmcnt(6)
	v_cvt_pk_f32_fp8_e32 v[60:61], v70
	v_cvt_pk_f32_fp8_sdwa v[66:67], v70 src0_sel:WORD_1
	s_waitcnt vmcnt(4)
	v_cvt_pk_f32_fp8_e32 v[72:73], v74
	v_add_f32_e32 v58, v58, v64
	v_cvt_pk_f32_fp8_sdwa v[64:65], v68 src0_sel:WORD_1
	v_cvt_pk_f32_fp8_e32 v[68:69], v71
	v_cvt_pk_f32_fp8_sdwa v[70:71], v71 src0_sel:WORD_1
	v_add_f32_e32 v58, v58, v62
	v_pk_add_f32 v[22:23], v[22:23], v[42:43]
	v_pk_add_f32 v[24:25], v[24:25], v[44:45]
	v_pk_add_f32 v[28:29], v[28:29], v[56:57]
	v_add_f32_e32 v45, v58, v72
	v_pk_add_f32 v[40:41], v[40:41], v[46:47]
	v_pk_add_f32 v[26:27], v[26:27], v[52:53]
	v_pk_mov_b32 v[46:47], v[60:61], v[66:67] op_sel:[1,0]
	v_mov_b32_e32 v61, v59
	s_waitcnt vmcnt(3)
	v_cvt_pk_f32_fp8_e32 v[52:53], v76
	s_waitcnt vmcnt(2)
	v_cvt_pk_f32_fp8_e32 v[56:57], v77
	v_cvt_pk_f32_fp8_sdwa v[58:59], v77 src0_sel:WORD_1
	v_cvt_pk_f32_fp8_sdwa v[74:75], v74 src0_sel:WORD_1
	v_pk_add_f32 v[42:43], v[50:51], v[54:55]
	v_mov_b32_e32 v50, v69
	v_mov_b32_e32 v51, v71
	v_mov_b32_e32 v69, v64
	v_mov_b32_e32 v71, v65
	v_cvt_pk_f32_fp8_sdwa v[54:55], v76 src0_sel:WORD_1
	v_pk_add_f32 v[22:23], v[22:23], v[46:47]
	s_waitcnt vmcnt(1)
	v_cvt_pk_f32_fp8_e32 v[46:47], v78
	v_cvt_pk_f32_fp8_sdwa v[64:65], v78 src0_sel:WORD_1
	v_pk_add_f32 v[24:25], v[24:25], v[50:51]
	s_waitcnt vmcnt(0)
	v_cvt_pk_f32_fp8_e32 v[50:51], v79
	v_add_f32_e32 v39, v39, v67
	v_cvt_pk_f32_fp8_sdwa v[66:67], v79 src0_sel:WORD_1
	v_pk_add_f32 v[48:49], v[48:49], v[60:61]
	v_pk_add_f32 v[40:41], v[40:41], v[52:53]
	v_pk_mov_b32 v[52:53], v[56:57], v[58:59] op_sel:[1,0]
	v_mov_b32_e32 v57, v63
	v_pk_add_f32 v[42:43], v[42:43], v[68:69]
	v_pk_add_f32 v[26:27], v[26:27], v[54:55]
	v_add_f32_e32 v55, v39, v59
	v_mov_b32_e32 v58, v47
	v_mov_b32_e32 v59, v65
	v_mov_b32_e32 v47, v74
	v_pk_add_f32 v[22:23], v[22:23], v[52:53]
	v_pk_mul_f32 v[52:53], v[40:41], v[40:41]
	v_pk_add_f32 v[48:49], v[48:49], v[56:57]
	v_pk_add_f32 v[28:29], v[28:29], v[70:71]
	v_mov_b32_e32 v65, v75
	v_pk_add_f32 v[24:25], v[24:25], v[58:59]
	v_pk_mul_f32 v[58:59], v[26:27], v[26:27]
	v_pk_add_f32 v[42:43], v[42:43], v[46:47]
	v_mov_b32_e32 v44, v52
	v_pk_mov_b32 v[52:53], v[52:53], v[50:51] op_sel:[1,0]
	v_mov_b32_e32 v72, v48
	v_mov_b32_e32 v63, v66
	v_pk_add_f32 v[28:29], v[28:29], v[64:65]
	v_pk_mul_f32 v[46:47], v[22:23], v[22:23]
	v_pk_mov_b32 v[64:65], v[58:59], v[50:51] op_sel:[1,0]
	v_pk_mul_f32 v[68:69], v[48:49], v[48:49]
	v_mov_b32_e32 v62, v42
	v_pk_add_f32 v[52:53], v[44:45], v[52:53]
	v_mov_b32_e32 v44, v58
	v_pk_add_f32 v[58:59], v[48:49], v[72:73]
	v_mov_b32_e32 v61, v51
	v_mul_f32_e32 v60, v55, v55
	v_pk_mul_f32 v[56:57], v[24:25], v[24:25]
	v_mov_b32_e32 v66, v28
	v_mov_b32_e32 v54, v23
	v_mov_b32_e32 v50, v46
	v_pk_add_f32 v[62:63], v[42:43], v[62:63]
	v_mov_b32_e32 v49, v22
	v_pk_add_f32 v[22:23], v[44:45], v[64:65]
	v_mov_b32_e32 v69, v59
	v_mov_b32_e32 v58, v47
	v_pk_add_f32 v[66:67], v[28:29], v[66:67]
	v_pk_fma_f32 v[70:71], v[42:43], v[42:43], v[56:57]
	v_pk_fma_f32 v[56:57], v[28:29], v[28:29], v[56:57] op_sel:[0,0,1] op_sel_hi:[1,1,0]
	v_mov_b32_e32 v43, v24
	v_mov_b32_e32 v29, v25
	v_pk_mul_f32 v[24:25], v[62:63], v[62:63]
	v_pk_add_f32 v[46:47], v[68:69], v[50:51]
	v_pk_add_f32 v[50:51], v[58:59], v[60:61]
	v_pk_add_f32 v[58:59], v[52:53], v[22:23]
	v_pk_mul_f32 v[22:23], v[52:53], v[22:23]
	v_pk_mul_f32 v[44:45], v[66:67], v[66:67]
	v_mov_b32_e32 v71, v25
	v_mov_b32_e32 v59, v23
	v_pk_add_f32 v[22:23], v[46:47], v[50:51]
	v_pk_mul_f32 v[24:25], v[46:47], v[50:51]
	v_mov_b32_e32 v57, v45
	v_mov_b32_e32 v23, v25
	v_pk_add_f32 v[44:45], v[70:71], v[56:57]
	v_pk_add_f32 v[22:23], v[58:59], v[22:23]
	v_mov_b32_e32 v66, v63
	v_pk_add_f32 v[22:23], v[22:23], v[44:45]
	v_mov_b32_e32 v46, v53
	v_add_f32_e32 v22, v22, v23
	s_nop 1
	v_add_f32_dpp v22, v22, v22 quad_perm:[1,0,3,2] row_mask:0xf bank_mask:0xf
	s_nop 1
	v_add_f32_dpp v22, v22, v22 quad_perm:[2,3,0,1] row_mask:0xf bank_mask:0xf
	s_nop 1
	v_add_f32_dpp v22, v22, v22 row_half_mirror row_mask:0xf bank_mask:0xf
	s_nop 1
	v_add_f32_dpp v22, v22, v22 row_mirror row_mask:0xf bank_mask:0xf
	v_mov_b32_e32 v23, v22
	s_nop 1
	v_permlane16_swap_b32 v22, v23
	v_add_f32_e32 v22, v22, v23
	v_mov_b32_e32 v23, v22
	s_nop 1
	v_permlane32_swap_b32 v22, v23
	v_add_f32_e32 v22, v22, v23
	v_fmamk_f32 v22, v22, 0x3a800000, v37
	v_mul_f32_e32 v23, 0x4f800000, v22
	v_cmp_gt_f32_e32 vcc, s7, v22
	s_nop 1
	v_cndmask_b32_e32 v22, v22, v23, vcc
	v_sqrt_f32_e32 v23, v22
	s_nop 0
	v_add_u32_e32 v24, -1, v23
	v_add_u32_e32 v25, 1, v23
	v_fma_f32 v39, -v24, v23, v22
	v_fma_f32 v44, -v25, v23, v22
	v_cmp_ge_f32_e64 s[0:1], 0, v39
	s_nop 1
	v_cndmask_b32_e64 v23, v23, v24, s[0:1]
	v_cmp_lt_f32_e64 s[0:1], 0, v44
	s_nop 1
	v_cndmask_b32_e64 v23, v23, v25, s[0:1]
	v_mul_f32_e32 v24, 0x37800000, v23
	v_cndmask_b32_e32 v23, v23, v24, vcc
	v_cmp_class_f32_e32 vcc, v22, v38
	s_nop 1
	v_cndmask_b32_e32 v22, v23, v22, vcc
	v_div_scale_f32 v23, s[0:1], v22, v22, 1.0
	v_rcp_f32_e32 v25, v23
	v_div_scale_f32 v24, vcc, 1.0, v22, 1.0
	v_fma_f32 v39, -v23, v25, 1.0
	v_fmac_f32_e32 v25, v39, v25
	v_mul_f32_e32 v39, v24, v25
	v_fma_f32 v44, -v23, v39, v24
	v_fmac_f32_e32 v39, v44, v25
	v_fma_f32 v23, -v23, v39, v24
	v_div_fmas_f32 v23, v23, v25, v39
	v_div_fixup_f32 v22, v23, v22, 1.0
	v_pk_mul_f32 v[40:41], v[40:41], v[22:23] op_sel_hi:[1,0]
	v_pk_mul_f32 v[24:25], v[26:27], v[22:23] op_sel_hi:[1,0]
	v_pk_mul_f32 v[26:27], v[48:49], v[22:23] op_sel_hi:[1,0]
	v_pk_mul_f32 v[44:45], v[54:55], v[22:23] op_sel_hi:[1,0]
	v_pk_mul_f32 v[48:49], v[42:43], v[22:23] op_sel_hi:[1,0]
	v_pk_mul_f32 v[42:43], v[28:29], v[22:23] op_sel_hi:[1,0]
	v_pk_mul_f32 v[50:51], v[46:47], v[22:23] op_sel_hi:[1,0]
	v_pk_mul_f32 v[46:47], v[66:67], v[22:23] op_sel_hi:[1,0]
	v_pk_mul_f32 v[24:25], v[2:3], v[24:25]
	v_pk_mul_f32 v[22:23], v[0:1], v[40:41]
	v_pk_mul_f32 v[28:29], v[6:7], v[44:45]
	v_pk_mul_f32 v[26:27], v[4:5], v[26:27]
	v_pk_mul_f32 v[42:43], v[10:11], v[42:43]
	v_pk_mul_f32 v[40:41], v[8:9], v[48:49]
	v_pk_mul_f32 v[46:47], v[14:15], v[46:47]
	v_pk_mul_f32 v[44:45], v[12:13], v[50:51]
	global_store_dwordx4 v[18:19], v[22:25], off offset:-3072
	global_store_dwordx4 v[18:19], v[26:29], off offset:-2048
	global_store_dwordx4 v[18:19], v[40:43], off offset:-1024
	global_store_dwordx4 v[18:19], v[44:47], off
	v_lshl_add_u64 v[18:19], v[18:19], 0, s[12:13]
	s_cbranch_scc1 .LBB0_2192
